# barrier spin loops poll without the 64-clock sleep
# speedup vs baseline: 1.0001x; 1.0001x over previous
; __device__ __forceinline__ unsigned xb_ld(unsigned* p)              { return __hip_atomic_load(p, __ATOMIC_RELAXED, __HIP_MEMORY_SCOPE_AGENT); }
; __device__ __forceinline__ void xcd_barrier_complete(unsigned* bar, unsigned x, unsigned& nloc, unsigned& nx) {
;     const unsigned G = gridDim.x * gridDim.y * gridDim.z;
;     unsigned sum, cnt, mine, sp = 0u;
;     for (;;) {
;         sum = 0u; cnt = 0u; mine = 0u;
; #pragma unroll
;         for (unsigned j = 0; j < 16; ++j) { const unsigned c = xb_ld(&bar[XB_XCNT(j)]); sum += c; cnt += (c > 0u) ? 1u : 0u; mine = (j == x) ? c : mine; }
;         if (sum == G) break;
;         __builtin_amdgcn_s_sleep(1);
;         if ((++sp & 255u) == 0u) { if (xb_ld(&bar[XB_TMO])) break; if (sp > XB_SPIN_CAP) { atomicAdd(&bar[XB_TMO], 1u); break; } }
;     }
.LBB0_55:
	global_load_dword v17, v18, s[8:9] sc1
	global_load_dword v2, v18, s[10:11] sc1
	global_load_dword v3, v18, s[12:13] sc1
	global_load_dword v4, v18, s[14:15] sc1
	global_load_dword v5, v18, s[16:17] sc1
	global_load_dword v6, v18, s[18:19] sc1
	global_load_dword v7, v18, s[20:21] sc1
	global_load_dword v8, v18, s[22:23] sc1
	global_load_dword v9, v18, s[24:25] sc1
	global_load_dword v10, v18, s[26:27] sc1
	global_load_dword v11, v18, s[28:29] sc1
	global_load_dword v12, v18, s[30:31] sc1
	global_load_dword v13, v18, s[34:35] sc1
	global_load_dword v14, v18, s[36:37] sc1
	global_load_dword v15, v18, s[38:39] sc1
	global_load_dword v16, v18, s[40:41] sc1
	s_mov_b64 s[42:43], -1
	s_mov_b64 s[44:45], -1
	s_waitcnt vmcnt(14)
	v_add_u32_e32 v19, v2, v17
	s_waitcnt vmcnt(13)
	v_add_u32_e32 v19, v19, v3
	s_waitcnt vmcnt(12)
	v_add_u32_e32 v19, v19, v4
	s_waitcnt vmcnt(11)
	v_add_u32_e32 v19, v19, v5
	s_waitcnt vmcnt(10)
	v_add_u32_e32 v19, v19, v6
	s_waitcnt vmcnt(9)
	v_add_u32_e32 v19, v19, v7
	s_waitcnt vmcnt(8)
	v_add_u32_e32 v19, v19, v8
	s_waitcnt vmcnt(7)
	v_add_u32_e32 v19, v19, v9
	s_waitcnt vmcnt(6)
	v_add_u32_e32 v19, v19, v10
	s_waitcnt vmcnt(5)
	v_add_u32_e32 v19, v19, v11
	s_waitcnt vmcnt(4)
	v_add_u32_e32 v19, v19, v12
	s_waitcnt vmcnt(3)
	v_add_u32_e32 v19, v19, v13
	s_waitcnt vmcnt(2)
	v_add_u32_e32 v19, v19, v14
	s_waitcnt vmcnt(1)
	v_add_u32_e32 v19, v19, v15
	s_waitcnt vmcnt(0)
	v_add_u32_e32 v19, v19, v16
	v_cmp_eq_u32_e32 vcc, s33, v19
	s_cbranch_vccnz .LBB0_54
	s_and_b32 s42, s48, 0xff
	s_cmp_eq_u32 s42, 0
	s_mov_b64 s[42:43], -1
	s_mov_b64 s[46:47], -1
	s_nop 0
	s_cbranch_scc0 .LBB0_59
	global_load_dword v19, v18, s[6:7] sc1
	s_waitcnt vmcnt(0)
	v_cmp_eq_u32_e32 vcc, 0, v19
	s_cbranch_vccnz .LBB0_61
	s_mov_b64 s[46:47], 0

; __device__ __forceinline__ unsigned xb_ld(unsigned* p)              { return __hip_atomic_load(p, __ATOMIC_RELAXED, __HIP_MEMORY_SCOPE_AGENT); }
; __device__ __forceinline__ unsigned xb_add(unsigned* p, unsigned v) { return __hip_atomic_fetch_add(p, v, __ATOMIC_RELAXED, __HIP_MEMORY_SCOPE_AGENT); }
; #define XB_SPIN(cond, bar) do { unsigned _sp = 0; while (cond) { __builtin_amdgcn_s_sleep(1); \
;     if ((++_sp & 255u) == 0u) { if (xb_ld(&(bar)[XB_TMO])) break; if (_sp > XB_SPIN_CAP) { atomicAdd(&(bar)[XB_TMO], 1u); break; } } } } while (0)
; __device__ __forceinline__ void xcd_barrier(const XcdBarrier& b) {
;     ...
;             const unsigned tg = og / nx;
;             if (og + 1u == (tg + 1u) * nx) xb_add(&bar[XB_TOPGEN], 1u);
;             else XB_SPIN(xb_ld(&bar[XB_TOPGEN]) == tg, bar);
;             __builtin_amdgcn_fence(__ATOMIC_ACQUIRE, "agent");
;             xb_add(&bar[XB_XGEN(b.x)], 1u);
;             asm volatile("s_waitcnt vmcnt(0)" ::: "memory");
;         } else {
;             XB_SPIN(xb_ld(&bar[XB_XGEN(b.x)]) == gen, bar);
;             __builtin_amdgcn_fence(__ATOMIC_ACQUIRE, "agent");
;             asm volatile("s_waitcnt vmcnt(0)" ::: "memory");
.LBB0_71:
	s_and_b32 s22, s26, 0xff
	s_mov_b64 s[20:21], -1
	s_cmp_lg_u32 s22, 0
	s_mov_b64 s[24:25], -1
	s_nop 0
	s_cbranch_scc1 .LBB0_74
	global_load_dword v4, v2, s[12:13] sc1
	s_waitcnt vmcnt(0)
	v_cmp_eq_u32_e32 vcc, 0, v4
	s_cbranch_vccnz .LBB0_76
	s_mov_b64 s[24:25], 0
	s_mov_b64 s[22:23], -1

; __device__ __forceinline__ unsigned xb_ld(unsigned* p)              { return __hip_atomic_load(p, __ATOMIC_RELAXED, __HIP_MEMORY_SCOPE_AGENT); }
; __device__ __forceinline__ unsigned xb_add(unsigned* p, unsigned v) { return __hip_atomic_fetch_add(p, v, __ATOMIC_RELAXED, __HIP_MEMORY_SCOPE_AGENT); }
; #define XB_SPIN(cond, bar) do { unsigned _sp = 0; while (cond) { __builtin_amdgcn_s_sleep(1); \
;     if ((++_sp & 255u) == 0u) { if (xb_ld(&(bar)[XB_TMO])) break; if (_sp > XB_SPIN_CAP) { atomicAdd(&(bar)[XB_TMO], 1u); break; } } } } while (0)
; __device__ __forceinline__ void xcd_barrier(const XcdBarrier& b) {
;     ...
;             const unsigned tg = og / nx;
;             if (og + 1u == (tg + 1u) * nx) xb_add(&bar[XB_TOPGEN], 1u);
;             else XB_SPIN(xb_ld(&bar[XB_TOPGEN]) == tg, bar);
;             __builtin_amdgcn_fence(__ATOMIC_ACQUIRE, "agent");
;             xb_add(&bar[XB_XGEN(b.x)], 1u);
;             asm volatile("s_waitcnt vmcnt(0)" ::: "memory");
;         } else {
;             XB_SPIN(xb_ld(&bar[XB_XGEN(b.x)]) == gen, bar);
;             __builtin_amdgcn_fence(__ATOMIC_ACQUIRE, "agent");
;             asm volatile("s_waitcnt vmcnt(0)" ::: "memory");
.LBB0_88:
	s_and_b32 s20, s26, 0xff
	s_cmp_lg_u32 s20, 0
	s_mov_b64 s[22:23], -1
	s_nop 0
	s_cbranch_scc1 .LBB0_91
	global_load_dword v3, v2, s[12:13] sc1
	s_waitcnt vmcnt(0)
	v_cmp_eq_u32_e32 vcc, 0, v3
	s_cbranch_vccnz .LBB0_93
	s_mov_b64 s[22:23], 0
	s_mov_b64 s[20:21], -1

; __device__ __forceinline__ unsigned xb_ld(unsigned* p)              { return __hip_atomic_load(p, __ATOMIC_RELAXED, __HIP_MEMORY_SCOPE_AGENT); }
; __device__ __forceinline__ void xcd_barrier_complete(unsigned* bar, unsigned x, unsigned& nloc, unsigned& nx) {
;     ...
;     for (;;) {
;         sum = 0u; cnt = 0u; mine = 0u;
; #pragma unroll
;         for (unsigned j = 0; j < 16; ++j) { const unsigned c = xb_ld(&bar[XB_XCNT(j)]); sum += c; cnt += (c > 0u) ? 1u : 0u; mine = (j == x) ? c : mine; }
;         if (sum == G) break;
;         __builtin_amdgcn_s_sleep(1);
;         if ((++sp & 255u) == 0u) { if (xb_ld(&bar[XB_TMO])) break; if (sp > XB_SPIN_CAP) { atomicAdd(&bar[XB_TMO], 1u); break; } }
;     }
.LBB0_385:
	global_load_dword v17, v18, s[8:9] sc1
	global_load_dword v2, v18, s[10:11] sc1
	global_load_dword v3, v18, s[12:13] sc1
	global_load_dword v4, v18, s[14:15] sc1
	global_load_dword v5, v18, s[16:17] sc1
	global_load_dword v6, v18, s[18:19] sc1
	global_load_dword v7, v18, s[20:21] sc1
	global_load_dword v8, v18, s[22:23] sc1
	global_load_dword v9, v18, s[26:27] sc1
	global_load_dword v10, v18, s[28:29] sc1
	global_load_dword v11, v18, s[30:31] sc1
	global_load_dword v12, v18, s[34:35] sc1
	global_load_dword v13, v18, s[36:37] sc1
	global_load_dword v14, v18, s[38:39] sc1
	global_load_dword v15, v18, s[40:41] sc1
	global_load_dword v16, v18, s[42:43] sc1
	s_mov_b64 s[44:45], -1
	s_mov_b64 s[46:47], -1
	s_waitcnt vmcnt(14)
	v_add_u32_e32 v19, v2, v17
	s_waitcnt vmcnt(13)
	v_add_u32_e32 v19, v19, v3
	s_waitcnt vmcnt(12)
	v_add_u32_e32 v19, v19, v4
	s_waitcnt vmcnt(11)
	v_add_u32_e32 v19, v19, v5
	s_waitcnt vmcnt(10)
	v_add_u32_e32 v19, v19, v6
	s_waitcnt vmcnt(9)
	v_add_u32_e32 v19, v19, v7
	s_waitcnt vmcnt(8)
	v_add_u32_e32 v19, v19, v8
	s_waitcnt vmcnt(7)
	v_add_u32_e32 v19, v19, v9
	s_waitcnt vmcnt(6)
	v_add_u32_e32 v19, v19, v10
	s_waitcnt vmcnt(5)
	v_add_u32_e32 v19, v19, v11
	s_waitcnt vmcnt(4)
	v_add_u32_e32 v19, v19, v12
	s_waitcnt vmcnt(3)
	v_add_u32_e32 v19, v19, v13
	s_waitcnt vmcnt(2)
	v_add_u32_e32 v19, v19, v14
	s_waitcnt vmcnt(1)
	v_add_u32_e32 v19, v19, v15
	s_waitcnt vmcnt(0)
	v_add_u32_e32 v19, v19, v16
	v_cmp_eq_u32_e32 vcc, s33, v19
	s_cbranch_vccnz .LBB0_384
	s_and_b32 s44, s50, 0xff
	s_cmp_eq_u32 s44, 0
	s_mov_b64 s[44:45], -1
	s_mov_b64 s[48:49], -1
	s_nop 0
	s_cbranch_scc0 .LBB0_389
	global_load_dword v19, v18, s[6:7] sc1
	s_waitcnt vmcnt(0)
	v_cmp_eq_u32_e32 vcc, 0, v19
	s_cbranch_vccnz .LBB0_391
	s_mov_b64 s[48:49], 0

; __device__ __forceinline__ unsigned xb_ld(unsigned* p)              { return __hip_atomic_load(p, __ATOMIC_RELAXED, __HIP_MEMORY_SCOPE_AGENT); }
; __device__ __forceinline__ unsigned xb_add(unsigned* p, unsigned v) { return __hip_atomic_fetch_add(p, v, __ATOMIC_RELAXED, __HIP_MEMORY_SCOPE_AGENT); }
; #define XB_SPIN(cond, bar) do { unsigned _sp = 0; while (cond) { __builtin_amdgcn_s_sleep(1); \
;     if ((++_sp & 255u) == 0u) { if (xb_ld(&(bar)[XB_TMO])) break; if (_sp > XB_SPIN_CAP) { atomicAdd(&(bar)[XB_TMO], 1u); break; } } } } while (0)
; __device__ __forceinline__ void xcd_barrier(const XcdBarrier& b) {
;     ...
;             const unsigned tg = og / nx;
;             if (og + 1u == (tg + 1u) * nx) xb_add(&bar[XB_TOPGEN], 1u);
;             else XB_SPIN(xb_ld(&bar[XB_TOPGEN]) == tg, bar);
;             __builtin_amdgcn_fence(__ATOMIC_ACQUIRE, "agent");
;             xb_add(&bar[XB_XGEN(b.x)], 1u);
;             asm volatile("s_waitcnt vmcnt(0)" ::: "memory");
;         } else {
;             XB_SPIN(xb_ld(&bar[XB_XGEN(b.x)]) == gen, bar);
;             __builtin_amdgcn_fence(__ATOMIC_ACQUIRE, "agent");
;             asm volatile("s_waitcnt vmcnt(0)" ::: "memory");
.LBB0_401:
	s_and_b32 s22, s28, 0xff
	s_mov_b64 s[20:21], -1
	s_cmp_lg_u32 s22, 0
	s_mov_b64 s[26:27], -1
	s_nop 0
	s_cbranch_scc1 .LBB0_404
	global_load_dword v4, v2, s[12:13] sc1
	s_waitcnt vmcnt(0)
	v_cmp_eq_u32_e32 vcc, 0, v4
	s_cbranch_vccnz .LBB0_406
	s_mov_b64 s[26:27], 0
	s_mov_b64 s[22:23], -1

; __device__ __forceinline__ unsigned xb_ld(unsigned* p)              { return __hip_atomic_load(p, __ATOMIC_RELAXED, __HIP_MEMORY_SCOPE_AGENT); }
; __device__ __forceinline__ unsigned xb_add(unsigned* p, unsigned v) { return __hip_atomic_fetch_add(p, v, __ATOMIC_RELAXED, __HIP_MEMORY_SCOPE_AGENT); }
; #define XB_SPIN(cond, bar) do { unsigned _sp = 0; while (cond) { __builtin_amdgcn_s_sleep(1); \
;     if ((++_sp & 255u) == 0u) { if (xb_ld(&(bar)[XB_TMO])) break; if (_sp > XB_SPIN_CAP) { atomicAdd(&(bar)[XB_TMO], 1u); break; } } } } while (0)
; __device__ __forceinline__ void xcd_barrier(const XcdBarrier& b) {
;     ...
;             const unsigned tg = og / nx;
;             if (og + 1u == (tg + 1u) * nx) xb_add(&bar[XB_TOPGEN], 1u);
;             else XB_SPIN(xb_ld(&bar[XB_TOPGEN]) == tg, bar);
;             __builtin_amdgcn_fence(__ATOMIC_ACQUIRE, "agent");
;             xb_add(&bar[XB_XGEN(b.x)], 1u);
;             asm volatile("s_waitcnt vmcnt(0)" ::: "memory");
;         } else {
;             XB_SPIN(xb_ld(&bar[XB_XGEN(b.x)]) == gen, bar);
;             __builtin_amdgcn_fence(__ATOMIC_ACQUIRE, "agent");
;             asm volatile("s_waitcnt vmcnt(0)" ::: "memory");
.LBB0_418:
	s_and_b32 s20, s28, 0xff
	s_cmp_lg_u32 s20, 0
	s_mov_b64 s[22:23], -1
	s_nop 0
	s_cbranch_scc1 .LBB0_421
	global_load_dword v3, v2, s[12:13] sc1
	s_waitcnt vmcnt(0)
	v_cmp_eq_u32_e32 vcc, 0, v3
	s_cbranch_vccnz .LBB0_423
	s_mov_b64 s[22:23], 0
	s_mov_b64 s[20:21], -1

; __device__ __forceinline__ unsigned xb_ld(unsigned* p)              { return __hip_atomic_load(p, __ATOMIC_RELAXED, __HIP_MEMORY_SCOPE_AGENT); }
; __device__ __forceinline__ void xcd_barrier_complete(unsigned* bar, unsigned x, unsigned& nloc, unsigned& nx) {
;     ...
;     for (;;) {
;         sum = 0u; cnt = 0u; mine = 0u;
; #pragma unroll
;         for (unsigned j = 0; j < 16; ++j) { const unsigned c = xb_ld(&bar[XB_XCNT(j)]); sum += c; cnt += (c > 0u) ? 1u : 0u; mine = (j == x) ? c : mine; }
;         if (sum == G) break;
;         __builtin_amdgcn_s_sleep(1);
;         if ((++sp & 255u) == 0u) { if (xb_ld(&bar[XB_TMO])) break; if (sp > XB_SPIN_CAP) { atomicAdd(&bar[XB_TMO], 1u); break; } }
;     }
.LBB0_942:
	global_load_dword v17, v18, s[10:11] sc1
	global_load_dword v2, v18, s[12:13] sc1
	global_load_dword v3, v18, s[14:15] sc1
	global_load_dword v4, v18, s[16:17] sc1
	global_load_dword v5, v18, s[18:19] sc1
	global_load_dword v6, v18, s[20:21] sc1
	global_load_dword v7, v18, s[22:23] sc1
	global_load_dword v8, v18, s[24:25] sc1
	global_load_dword v9, v18, s[26:27] sc1
	global_load_dword v10, v18, s[28:29] sc1
	global_load_dword v11, v18, s[30:31] sc1
	global_load_dword v12, v18, s[34:35] sc1
	global_load_dword v13, v18, s[36:37] sc1
	global_load_dword v14, v18, s[38:39] sc1
	global_load_dword v15, v18, s[40:41] sc1
	global_load_dword v16, v18, s[42:43] sc1
	s_mov_b64 s[44:45], -1
	s_mov_b64 s[46:47], -1
	s_waitcnt vmcnt(14)
	v_add_u32_e32 v19, v2, v17
	s_waitcnt vmcnt(13)
	v_add_u32_e32 v19, v19, v3
	s_waitcnt vmcnt(12)
	v_add_u32_e32 v19, v19, v4
	s_waitcnt vmcnt(11)
	v_add_u32_e32 v19, v19, v5
	s_waitcnt vmcnt(10)
	v_add_u32_e32 v19, v19, v6
	s_waitcnt vmcnt(9)
	v_add_u32_e32 v19, v19, v7
	s_waitcnt vmcnt(8)
	v_add_u32_e32 v19, v19, v8
	s_waitcnt vmcnt(7)
	v_add_u32_e32 v19, v19, v9
	s_waitcnt vmcnt(6)
	v_add_u32_e32 v19, v19, v10
	s_waitcnt vmcnt(5)
	v_add_u32_e32 v19, v19, v11
	s_waitcnt vmcnt(4)
	v_add_u32_e32 v19, v19, v12
	s_waitcnt vmcnt(3)
	v_add_u32_e32 v19, v19, v13
	s_waitcnt vmcnt(2)
	v_add_u32_e32 v19, v19, v14
	s_waitcnt vmcnt(1)
	v_add_u32_e32 v19, v19, v15
	s_waitcnt vmcnt(0)
	v_add_u32_e32 v19, v19, v16
	v_cmp_eq_u32_e32 vcc, s33, v19
	s_cbranch_vccnz .LBB0_941
	s_and_b32 s44, s50, 0xff
	s_cmp_eq_u32 s44, 0
	s_mov_b64 s[44:45], -1
	s_mov_b64 s[48:49], -1
	s_nop 0
	s_cbranch_scc0 .LBB0_946
	global_load_dword v19, v18, s[8:9] sc1
	s_waitcnt vmcnt(0)
	v_cmp_eq_u32_e32 vcc, 0, v19
	s_cbranch_vccnz .LBB0_948
	s_mov_b64 s[48:49], 0

; __device__ __forceinline__ unsigned xb_ld(unsigned* p)              { return __hip_atomic_load(p, __ATOMIC_RELAXED, __HIP_MEMORY_SCOPE_AGENT); }
; __device__ __forceinline__ unsigned xb_add(unsigned* p, unsigned v) { return __hip_atomic_fetch_add(p, v, __ATOMIC_RELAXED, __HIP_MEMORY_SCOPE_AGENT); }
; #define XB_SPIN(cond, bar) do { unsigned _sp = 0; while (cond) { __builtin_amdgcn_s_sleep(1); \
;     if ((++_sp & 255u) == 0u) { if (xb_ld(&(bar)[XB_TMO])) break; if (_sp > XB_SPIN_CAP) { atomicAdd(&(bar)[XB_TMO], 1u); break; } } } } while (0)
; __device__ __forceinline__ void xcd_barrier(const XcdBarrier& b) {
;     ...
;             const unsigned tg = og / nx;
;             if (og + 1u == (tg + 1u) * nx) xb_add(&bar[XB_TOPGEN], 1u);
;             else XB_SPIN(xb_ld(&bar[XB_TOPGEN]) == tg, bar);
;             __builtin_amdgcn_fence(__ATOMIC_ACQUIRE, "agent");
;             xb_add(&bar[XB_XGEN(b.x)], 1u);
;             asm volatile("s_waitcnt vmcnt(0)" ::: "memory");
;         } else {
;             XB_SPIN(xb_ld(&bar[XB_XGEN(b.x)]) == gen, bar);
;             __builtin_amdgcn_fence(__ATOMIC_ACQUIRE, "agent");
;             asm volatile("s_waitcnt vmcnt(0)" ::: "memory");
.LBB0_958:
	s_and_b32 s24, s28, 0xff
	s_mov_b64 s[22:23], -1
	s_cmp_lg_u32 s24, 0
	s_mov_b64 s[26:27], -1
	s_nop 0
	s_cbranch_scc1 .LBB0_961
	global_load_dword v4, v2, s[14:15] sc1
	s_waitcnt vmcnt(0)
	v_cmp_eq_u32_e32 vcc, 0, v4
	s_cbranch_vccnz .LBB0_963
	s_mov_b64 s[26:27], 0
	s_mov_b64 s[24:25], -1

; __device__ __forceinline__ unsigned xb_ld(unsigned* p)              { return __hip_atomic_load(p, __ATOMIC_RELAXED, __HIP_MEMORY_SCOPE_AGENT); }
; __device__ __forceinline__ unsigned xb_add(unsigned* p, unsigned v) { return __hip_atomic_fetch_add(p, v, __ATOMIC_RELAXED, __HIP_MEMORY_SCOPE_AGENT); }
; #define XB_SPIN(cond, bar) do { unsigned _sp = 0; while (cond) { __builtin_amdgcn_s_sleep(1); \
;     if ((++_sp & 255u) == 0u) { if (xb_ld(&(bar)[XB_TMO])) break; if (_sp > XB_SPIN_CAP) { atomicAdd(&(bar)[XB_TMO], 1u); break; } } } } while (0)
; __device__ __forceinline__ void xcd_barrier(const XcdBarrier& b) {
;     ...
;             const unsigned tg = og / nx;
;             if (og + 1u == (tg + 1u) * nx) xb_add(&bar[XB_TOPGEN], 1u);
;             else XB_SPIN(xb_ld(&bar[XB_TOPGEN]) == tg, bar);
;             __builtin_amdgcn_fence(__ATOMIC_ACQUIRE, "agent");
;             xb_add(&bar[XB_XGEN(b.x)], 1u);
;             asm volatile("s_waitcnt vmcnt(0)" ::: "memory");
;         } else {
;             XB_SPIN(xb_ld(&bar[XB_XGEN(b.x)]) == gen, bar);
;             __builtin_amdgcn_fence(__ATOMIC_ACQUIRE, "agent");
;             asm volatile("s_waitcnt vmcnt(0)" ::: "memory");
.LBB0_975:
	s_and_b32 s22, s28, 0xff
	s_cmp_lg_u32 s22, 0
	s_mov_b64 s[24:25], -1
	s_nop 0
	s_cbranch_scc1 .LBB0_978
	global_load_dword v3, v2, s[14:15] sc1
	s_waitcnt vmcnt(0)
	v_cmp_eq_u32_e32 vcc, 0, v3
	s_cbranch_vccnz .LBB0_980
	s_mov_b64 s[24:25], 0
	s_mov_b64 s[22:23], -1
